# baseline (speedup 1.0000x reference)
.LBB1_116:
	s_or_b64 exec, exec, s[14:15]
	v_mov_b32_e32 v50, v0
	s_lshr_b32 s0, s34, 13
	v_and_b32_e32 v52, 15, v50
	s_waitcnt lgkmcnt(0)
	v_lshlrev_b32_e32 v55, 2, v50
	v_lshlrev_b32_e32 v52, 6, v52
	v_and_b32_e32 v53, 48, v50
	v_lshlrev_b32_e32 v54, 6, v50
	v_and_b32_e32 v55, 32, v55
	v_bitop3_b32 v237, v52, v55, v53 bitop3:0x36
	v_and_b32_e32 v52, 0x3c0, v54
	v_lshlrev_b32_e32 v56, 7, v50
	v_bitop3_b32 v52, v52, v55, v53 bitop3:0x36
	v_and_or_b32 v238, v56, s23, v52
	v_lshlrev_b32_e32 v52, 8, v50
	v_lshlrev_b32_e32 v53, 3, v50
	v_lshlrev_b32_e32 v50, 4, v50
	v_and_b32_e32 v52, 0x400, v52
	v_and_b32_e32 v55, 0x1c0, v53
	v_and_b32_e32 v50, 48, v50
	s_and_b32 s0, s0, 0x3800
	v_or3_b32 v50, v52, v50, v55
	v_and_b32_e32 v52, 0xfffff000, v54
	s_bfe_u32 s17, s34, 0x80010
	s_mulk_i32 s0, 0xc00
	v_or_b32_e32 v239, v50, v52
	v_bitop3_b32 v240, v50, s30, v52 bitop3:0x36
	v_and_or_b32 v50, v53, s26, v52
	s_add_u32 s0, s4, s0
	v_add_u32_e32 v241, 0x8000, v50
	v_add_u32_e32 v50, 0x8200, v50
	s_addc_u32 s1, s5, 0
	s_lshl_b32 s35, s17, 7
	v_xor_b32_e32 v242, 32, v50
	s_cmp_lt_u32 s34, 0x8000000
	v_mov_b32_e32 v50, 0x24000
	v_mov_b32_e32 v170, 0
	v_and_b32_e32 v236, 0x4000, v54
	v_lshl_add_u32 v243, v51, 10, v50
	s_cselect_b32 s1, s1, s7
	s_cselect_b32 s0, s0, s6
	s_mov_b32 s36, 0
	s_xor_b64 s[2:3], s[12:13], -1
	v_mov_b32_e32 v234, v228
	s_mov_b32 s16, s21
	s_mov_b32 s37, 0
	v_mov_b32_e32 v171, v170
	v_mov_b32_e32 v172, v170
	v_mov_b32_e32 v173, v170
	v_mov_b32_e32 v162, v170
	v_mov_b32_e32 v163, v170
	v_mov_b32_e32 v164, v170
	v_mov_b32_e32 v165, v170
	v_mov_b32_e32 v174, v170
	v_mov_b32_e32 v175, v170
	v_mov_b32_e32 v176, v170
	v_mov_b32_e32 v177, v170
	v_mov_b32_e32 v166, v170
	v_mov_b32_e32 v167, v170
	v_mov_b32_e32 v168, v170
	v_mov_b32_e32 v169, v170
	v_mov_b32_e32 v154, v170
	v_mov_b32_e32 v155, v170
	v_mov_b32_e32 v156, v170
	v_mov_b32_e32 v157, v170
	v_mov_b32_e32 v146, v170
	v_mov_b32_e32 v147, v170
	v_mov_b32_e32 v148, v170
	v_mov_b32_e32 v149, v170
	v_mov_b32_e32 v158, v170
	v_mov_b32_e32 v159, v170
	v_mov_b32_e32 v160, v170
	v_mov_b32_e32 v161, v170
	v_mov_b32_e32 v150, v170
	v_mov_b32_e32 v151, v170
	v_mov_b32_e32 v152, v170
	v_mov_b32_e32 v153, v170
	v_mov_b32_e32 v138, v170
	v_mov_b32_e32 v139, v170
	v_mov_b32_e32 v140, v170
	v_mov_b32_e32 v141, v170
	v_mov_b32_e32 v130, v170
	v_mov_b32_e32 v131, v170
	v_mov_b32_e32 v132, v170
	v_mov_b32_e32 v133, v170
	v_mov_b32_e32 v142, v170
	v_mov_b32_e32 v143, v170
	v_mov_b32_e32 v144, v170
	v_mov_b32_e32 v145, v170
	v_mov_b32_e32 v134, v170
	v_mov_b32_e32 v135, v170
	v_mov_b32_e32 v136, v170
	v_mov_b32_e32 v137, v170
	v_mov_b32_e32 v122, v170
	v_mov_b32_e32 v123, v170
	v_mov_b32_e32 v124, v170
	v_mov_b32_e32 v125, v170
	v_mov_b32_e32 v114, v170
	v_mov_b32_e32 v115, v170
	v_mov_b32_e32 v116, v170
	v_mov_b32_e32 v117, v170
	v_mov_b32_e32 v126, v170
	v_mov_b32_e32 v127, v170
	v_mov_b32_e32 v128, v170
	v_mov_b32_e32 v129, v170
	v_mov_b32_e32 v118, v170
	v_mov_b32_e32 v119, v170
	v_mov_b32_e32 v120, v170
	v_mov_b32_e32 v121, v170
	v_mov_b32_e32 v106, v170
	v_mov_b32_e32 v107, v170
	v_mov_b32_e32 v108, v170
	v_mov_b32_e32 v109, v170
	v_mov_b32_e32 v98, v170
	v_mov_b32_e32 v99, v170
	v_mov_b32_e32 v100, v170
	v_mov_b32_e32 v101, v170
	v_mov_b32_e32 v110, v170
	v_mov_b32_e32 v111, v170
	v_mov_b32_e32 v112, v170
	v_mov_b32_e32 v113, v170
	v_mov_b32_e32 v102, v170
	v_mov_b32_e32 v103, v170
	v_mov_b32_e32 v104, v170
	v_mov_b32_e32 v105, v170
	v_mov_b32_e32 v90, v170
	v_mov_b32_e32 v91, v170
	v_mov_b32_e32 v92, v170
	v_mov_b32_e32 v93, v170
	v_mov_b32_e32 v82, v170
	v_mov_b32_e32 v83, v170
	v_mov_b32_e32 v84, v170
	v_mov_b32_e32 v85, v170
	v_mov_b32_e32 v94, v170
	v_mov_b32_e32 v95, v170
	v_mov_b32_e32 v96, v170
	v_mov_b32_e32 v97, v170
	v_mov_b32_e32 v86, v170
	v_mov_b32_e32 v87, v170
	v_mov_b32_e32 v88, v170
	v_mov_b32_e32 v89, v170
	v_mov_b32_e32 v74, v170
	v_mov_b32_e32 v75, v170
	v_mov_b32_e32 v76, v170
	v_mov_b32_e32 v77, v170
	v_mov_b32_e32 v66, v170
	v_mov_b32_e32 v67, v170
	v_mov_b32_e32 v68, v170
	v_mov_b32_e32 v69, v170
	v_mov_b32_e32 v78, v170
	v_mov_b32_e32 v79, v170
	v_mov_b32_e32 v80, v170
	v_mov_b32_e32 v81, v170
	v_mov_b32_e32 v70, v170
	v_mov_b32_e32 v71, v170
	v_mov_b32_e32 v72, v170
	v_mov_b32_e32 v73, v170
	v_mov_b32_e32 v62, v170
	v_mov_b32_e32 v63, v170
	v_mov_b32_e32 v64, v170
	v_mov_b32_e32 v65, v170
	v_mov_b32_e32 v54, v170
	v_mov_b32_e32 v55, v170
	v_mov_b32_e32 v56, v170
	v_mov_b32_e32 v57, v170
	v_mov_b32_e32 v58, v170
	v_mov_b32_e32 v59, v170
	v_mov_b32_e32 v60, v170
	v_mov_b32_e32 v61, v170
	v_mov_b32_e32 v50, v170
	v_mov_b32_e32 v51, v170
	v_mov_b32_e32 v52, v170
	v_mov_b32_e32 v53, v170
	s_branch .LBB1_118
	s_nop 0
	s_nop 0
